# v8s+meta with the hand-written attention loop shifted by 4 bytes (one s_nop ahead of the loop): code-placement phase test
# speedup vs baseline: 1.0013x; 1.0013x over previous
.LBB0_1088:
	v_lshlrev_b32_e32 v13, 3, v146
	v_and_b32_e32 v12, 0xc0, v12
	v_lshlrev_b32_e32 v14, 1, v146
	s_xor_b64 s[34:35], s[4:5], -1
	v_and_or_b32 v12, v13, 24, v12
	v_and_b32_e32 v14, 32, v14
	v_and_b32_e32 v13, 0x100, v13
	s_add_i32 s44, s44, s8
	v_or3_b32 v12, v12, v14, v13
	v_or_b32_e32 v13, s44, v145
	s_cmp_lg_u32 0, -1
	s_cselect_b32 s4, 0, 0
	s_lshr_b32 s46, s7, 6
	v_add_u32_e32 v163, 0xffffff91, v13
	v_lshlrev_b32_e32 v164, 4, v4
	v_lshlrev_b32_e32 v13, 4, v145
	s_add_i32 s38, 0, 0x10800
	s_add_i32 s47, s46, -2
	s_or_b32 s64, s44, 31
	v_and_b32_e32 v13, 0x70, v13
	v_add_u32_e32 v14, 32, v164
	v_lshl_add_u32 v171, v146, 2, s38
	s_lshl_b32 s38, s46, 8
	v_xad_u32 v168, v14, v13, 0
	v_add_u32_e32 v14, 64, v164
	s_add_u32 s38, s89, s38
	v_xad_u32 v169, v14, v13, 0
	v_add_u32_e32 v14, 0x60, v164
	s_addc_u32 s39, s88, 0
	s_and_b32 s7, s7, 0x1fc0
	s_add_i32 s6, s60, s6
	v_lshlrev_b32_e32 v144, 2, v4
	v_xad_u32 v166, v13, v164, 0
	v_xad_u32 v170, v14, v13, 0
	s_sub_i32 s65, s7, 64
	v_add_u32_e32 v13, s6, v145
	s_lshl_b32 s6, s46, 18
	v_ashrrev_i32_e32 v147, 31, v146
	v_sub_u32_e32 v13, v13, v144
	s_add_u32 s6, s90, s6
	v_lshl_add_u64 v[148:149], v[146:147], 2, s[38:39]
	v_subrev_u32_e32 v147, s7, v13
	s_addc_u32 s7, s91, 0
	v_add_u32_e32 v0, v0, v10
	v_lshl_add_u64 v[150:151], s[6:7], 0, v[0:1]
	v_add3_u32 v0, s61, v6, v11
	v_lshl_add_u64 v[152:153], s[6:7], 0, v[0:1]
	v_add_u32_e32 v0, v7, v5
	v_add3_u32 v0, v0, v8, v2
	v_lshl_or_b32 v0, v0, 12, v9
	v_add_u32_e32 v0, v0, v3
	v_lshl_add_u64 v[154:155], s[6:7], 0, v[0:1]
	v_add_u32_e32 v0, s62, v4
	v_lshlrev_b32_e32 v4, 1, v0
	s_mov_b32 s38, 0xffff0
	v_and_or_b32 v4, v4, s38, v5
	v_and_b32_e32 v0, 4, v0
	v_add_u32_e32 v162, s4, v12
	v_lshrrev_b32_e32 v12, 5, v146
	v_add_u32_e32 v0, v4, v0
	v_add_lshl_u32 v0, v0, v2, 12
	v_add_u16_e32 v2, 2, v12
	v_and_b32_e32 v2, 3, v2
	v_lshlrev_b32_e32 v2, 6, v2
	s_waitcnt vmcnt(0)
	v_or3_b32 v0, v0, v2, v3
	v_mov_b32_e32 v14, v1
	v_mov_b32_e32 v15, v1
	v_lshl_add_u64 v[156:157], s[6:7], 0, v[0:1]
	v_mov_b32_e32 v0, v1
	v_mov_b32_e32 v2, v1
	v_mov_b32_e32 v3, v1
	v_mov_b32_e32 v4, v1
	v_mov_b32_e32 v5, v1
	v_mov_b32_e32 v6, v1
	v_mov_b32_e32 v7, v1
	v_mov_b32_e32 v8, v1
	v_mov_b32_e32 v9, v1
	v_mov_b32_e32 v10, v1
	v_mov_b32_e32 v11, v1
	v_mov_b32_e32 v12, v1
	v_mov_b32_e32 v13, v1
	s_waitcnt lgkmcnt(0)
	v_mov_b64_e32 v[30:31], v[14:15]
	v_mov_b64_e32 v[46:47], v[14:15]
	v_mov_b64_e32 v[62:63], v[14:15]
	v_mov_b64_e32 v[78:79], v[14:15]
	s_mov_b32 s45, 0
	v_lshlrev_b32_e32 v165, 8, v145
	v_cmp_gt_u32_e64 s[4:5], 32, v146
	v_lshl_add_u32 v167, v145, 2, s54
	v_add_u32_e32 v161, s54, v164
	v_mov_b32_e32 v174, 0
	v_mov_b32_e32 v173, 0xf149f2ca
	s_mov_b32 s66, s46
	v_mov_b64_e32 v[28:29], v[12:13]
	v_mov_b64_e32 v[26:27], v[10:11]
	v_mov_b64_e32 v[24:25], v[8:9]
	v_mov_b64_e32 v[22:23], v[6:7]
	v_mov_b64_e32 v[20:21], v[4:5]
	v_mov_b64_e32 v[18:19], v[2:3]
	v_mov_b64_e32 v[16:17], v[0:1]
	v_mov_b64_e32 v[44:45], v[12:13]
	v_mov_b64_e32 v[42:43], v[10:11]
	v_mov_b64_e32 v[40:41], v[8:9]
	v_mov_b64_e32 v[38:39], v[6:7]
	v_mov_b64_e32 v[36:37], v[4:5]
	v_mov_b64_e32 v[34:35], v[2:3]
	v_mov_b64_e32 v[32:33], v[0:1]
	v_mov_b64_e32 v[60:61], v[12:13]
	v_mov_b64_e32 v[58:59], v[10:11]
	v_mov_b64_e32 v[56:57], v[8:9]
	v_mov_b64_e32 v[54:55], v[6:7]
	v_mov_b64_e32 v[52:53], v[4:5]
	v_mov_b64_e32 v[50:51], v[2:3]
	v_mov_b64_e32 v[48:49], v[0:1]
	v_mov_b64_e32 v[76:77], v[12:13]
	v_mov_b64_e32 v[74:75], v[10:11]
	v_mov_b64_e32 v[72:73], v[8:9]
	v_mov_b64_e32 v[70:71], v[6:7]
	v_mov_b64_e32 v[68:69], v[4:5]
	v_mov_b64_e32 v[66:67], v[2:3]
	v_mov_b64_e32 v[64:65], v[0:1]
	s_waitcnt vmcnt(0)
	s_barrier
	s_nop 0
	s_mov_b32 s45, 0
	s_lshl_b32 s65, s46, 6
	s_mov_b32 s66, 0
	s_mov_b32 s33, 0x8000
	s_mov_b32 s42, 0x11000
	s_mov_b32 s43, 0x15000
	s_mov_b32 s47, 0x19000
	s_mov_b32 s99, 0
	v_subrev_u32_e32 v147, 64, v147
	v_lshlrev_b32_e32 v232, 2, v146
	s_lshr_b32 s6, s68, 11
	s_and_b32 s7, s6, 3
	s_lshl_b32 s98, s7, 12
	s_lshl_b32 s7, s7, 16
	s_add_i32 s40, s46, -1
	s_lshl_b32 s41, s40, 8
	s_lshl_b32 s39, s40, 18
	s_add_u32 s40, s30, s41
	s_addc_u32 s41, s31, 0
	s_add_u32 s39, s39, s7
	v_and_b32_e32 v0, 15, v145
	v_lshlrev_b32_e32 v0, 4, v0
	v_xor_b32_e32 v0, v0, v164
	v_xad_u32 v166, v0, 0, v165
	v_xad_u32 v168, v0, 32, v165
	v_xad_u32 v169, v0, 64, v165
	s_movk_i32 s7, 0x60
	v_xad_u32 v170, v0, s7, v165
	s_movk_i32 s7, 0x80
	v_xad_u32 v251, v0, s7, v165
	s_movk_i32 s7, 0xa0
	v_xad_u32 v252, v0, s7, v165
	s_movk_i32 s7, 0xc0
	v_xad_u32 v253, v0, s7, v165
	s_movk_i32 s7, 0xe0
	v_xad_u32 v254, v0, s7, v165
	s_cmp_ge_u32 s6, 4
	s_cbranch_scc0 .Lat_setup_done
	s_add_u32 s100, s82, s39
	s_addc_u32 s101, s83, 0
	s_add_u32 s38, s84, s39
	s_addc_u32 s39, s85, 0
	v_lshrrev_b32_e32 v0, 4, v146
	v_and_b32_e32 v2, 15, v146
	v_xor_b32_e32 v2, v2, v0
	v_lshlrev_b32_e32 v2, 4, v2
	v_lshl_add_u32 v14, v0, 12, v2
	v_xor_b32_e32 v15, 64, v14
	v_add_u32_e32 v15, 0x4000, v15
	v_xor_b32_e32 v175, 0x80, v14
	v_add_u32_e32 v175, 0x8000, v175
	v_xor_b32_e32 v155, 0xc0, v14
	v_add_u32_e32 v155, 0xc000, v155
	v_bfe_u32 v0, v146, 4, 1
	v_bfe_u32 v2, v146, 2, 2
	v_lshl_add_u32 v0, v0, 3, v2
	v_lshlrev_b32_e32 v0, 12, v0
	v_lshrrev_b32_e32 v2, 5, v146
	v_lshl_add_u32 v0, v2, 6, v0
	v_and_b32_e32 v2, 3, v146
	v_lshl_add_u32 v228, v2, 4, v0
	v_add_u32_e32 v229, 0x80, v228
	v_add_u32_e32 v230, 0x4000, v228
	v_add_u32_e32 v231, 0x4080, v228
	s_add_i32 s6, s98, 0x4000
	s_mov_b32 s7, s6
	s_mov_b32 m0, s7
	s_add_i32 s7, s7, 0x400
	global_load_lds_dwordx4 v228, s[38:39]
	s_mov_b32 m0, s7
	s_add_i32 s7, s7, 0x400
	global_load_lds_dwordx4 v229, s[38:39]
	s_mov_b32 m0, s7
	s_add_i32 s7, s7, 0x400
	global_load_lds_dwordx4 v230, s[38:39]
	s_mov_b32 m0, s7
	s_nop 0
	global_load_lds_dwordx4 v231, s[38:39]
	s_sub_u32 s38, s38, 0x40000
	s_subb_u32 s39, s39, 0
	s_add_i32 s6, s42, s98
	s_mov_b32 s7, s6
	s_mov_b32 m0, s7
	s_add_i32 s7, s7, 0x400
	global_load_lds_dwordx4 v14, s[100:101]
	s_mov_b32 m0, s7
	s_add_i32 s7, s7, 0x400
	global_load_lds_dwordx4 v15, s[100:101]
	s_mov_b32 m0, s7
	s_add_i32 s7, s7, 0x400
	global_load_lds_dwordx4 v175, s[100:101]
	s_mov_b32 m0, s7
	s_nop 0
	global_load_lds_dwordx4 v155, s[100:101]
	global_load_dword v154, v232, s[40:41]
	s_sub_u32 s100, s100, 0x40000
	s_subb_u32 s101, s101, 0
	s_sub_u32 s40, s40, 0x100
	s_subb_u32 s41, s41, 0
	s_add_i32 s6, s43, s98
	s_mov_b32 s7, s6
	s_mov_b32 m0, s7
	s_add_i32 s7, s7, 0x400
	global_load_lds_dwordx4 v14, s[100:101]
	s_mov_b32 m0, s7
	s_add_i32 s7, s7, 0x400
	global_load_lds_dwordx4 v15, s[100:101]
	s_mov_b32 m0, s7
	s_add_i32 s7, s7, 0x400
	global_load_lds_dwordx4 v175, s[100:101]
	s_mov_b32 m0, s7
	s_nop 0
	global_load_lds_dwordx4 v155, s[100:101]
	global_load_dword v172, v232, s[40:41]
	s_sub_u32 s100, s100, 0x40000
	s_subb_u32 s101, s101, 0
	s_sub_u32 s40, s40, 0x100
	s_subb_u32 s41, s41, 0
	s_add_i32 s6, s47, s98
	s_mov_b32 s7, s6
	s_mov_b32 m0, s7
	s_add_i32 s7, s7, 0x400
	global_load_lds_dwordx4 v14, s[100:101]
	s_mov_b32 m0, s7
	s_add_i32 s7, s7, 0x400
	global_load_lds_dwordx4 v15, s[100:101]
	s_mov_b32 m0, s7
	s_add_i32 s7, s7, 0x400
	global_load_lds_dwordx4 v175, s[100:101]
	s_mov_b32 m0, s7
	s_nop 0
	global_load_lds_dwordx4 v155, s[100:101]
	global_load_dword v156, v232, s[40:41]
	s_sub_u32 s100, s100, 0x40000
	s_subb_u32 s101, s101, 0
	s_sub_u32 s40, s40, 0x100
	s_subb_u32 s41, s41, 0
	s_waitcnt vmcnt(0)
	s_cmp_lg_u32 s68, 0x2000
	s_cbranch_scc1 .Lat_setup_done
	v_add_u32_e32 v0, 256, v171
	ds_write_b32 v0, v154
	v_add_u32_e32 v0, 512, v171
	ds_write_b32 v0, v172
	v_add_u32_e32 v0, 768, v171
	ds_write_b32 v0, v156
	s_waitcnt lgkmcnt(0)
